# speedup vs baseline: 1.0052x; 1.0052x over previous
.LBB2_90:
	s_or_b64 exec, exec, s[4:5]
	s_load_dwordx2 s[34:35], s[0:1], 0x78
	s_load_dwordx2 s[36:37], s[0:1], 0x40
	v_ashrrev_i32_e32 v78, 2, v7
	v_and_b32_e32 v147, 48, v0
	v_cmp_lt_i32_e32 vcc, 0, v78
	s_and_saveexec_b64 s[40:41], vcc
	s_cbranch_execz .LBB2_101
	s_mov_b64 s[2:3], s[54:55]
	v_lshlrev_b32_e32 v152, 4, v131
	v_lshlrev_b32_e32 v2, 3, v131
	v_mov_b32_e32 v3, 0
	v_lshlrev_b32_e32 v2, 1, v2
	v_lshlrev_b32_e32 v79, 2, v84
	s_waitcnt lgkmcnt(0)
	v_lshl_add_u64 v[70:71], s[2:3], 0, v[2:3]
	v_or_b32_e32 v2, v147, v84
	v_lshlrev_b32_e32 v86, 2, v2
	v_lshlrev_b32_e32 v2, 2, v83
	v_and_b32_e32 v3, 0xc0, v6
	s_movk_i32 s2, 0x100
	v_or_b32_e32 v80, 64, v79
	v_or_b32_e32 v81, 0x80, v79
	v_or_b32_e32 v85, 0xc0, v79
	v_or_b32_e32 v87, 4, v86
	v_or_b32_e32 v88, 8, v86
	v_or_b32_e32 v89, 12, v86
	v_or_b32_e32 v90, 16, v86
	v_or_b32_e32 v91, 20, v86
	v_or_b32_e32 v92, 24, v86
	v_or_b32_e32 v93, 28, v86
	v_or_b32_e32 v94, 32, v86
	v_or_b32_e32 v95, 36, v86
	v_or_b32_e32 v96, 40, v86
	v_or_b32_e32 v97, 44, v86
	v_or_b32_e32 v98, 48, v86
	v_or_b32_e32 v99, 52, v86
	v_or_b32_e32 v100, 56, v86
	v_or_b32_e32 v101, 60, v86
	v_and_or_b32 v102, v2, s2, v3
	s_mov_b32 s33, 0
	s_mov_b64 s[42:43], 0
	s_movk_i32 s44, 0x110
	s_waitcnt vmcnt(0)
	v_mov_b32_e32 v105, v30
	v_mov_b32_e32 v103, v76
	v_mov_b32_e32 v104, v77
	s_branch .LBB2_93

.LBB2_95:
	s_or_b64 exec, exec, s[2:3]
	ds_bpermute_b32 v2, v86, v30
	ds_bpermute_b32 v3, v87, v30
	v_cmp_lt_i32_e64 s[18:19], 0, v76
	v_cmp_lt_i32_e64 s[20:21], 1, v76
	ds_bpermute_b32 v6, v88, v30
	s_waitcnt lgkmcnt(2)
	v_cndmask_b32_e64 v2, 0, v2, s[18:19]
	s_waitcnt lgkmcnt(1)
	v_cndmask_b32_e64 v4, 0, v3, s[20:21]
	s_nop 0
	s_nop 0
	v_lshl_add_u32 v2, v2, 8, v152
	v_lshl_add_u32 v4, v4, 8, v152
	s_nop 0
	s_nop 0
	global_load_dwordx4 v[42:45], v2, s[54:55]
	global_load_dwordx4 v[38:41], v4, s[54:55]
	ds_bpermute_b32 v4, v89, v30
	v_cmp_lt_i32_e64 s[26:27], 2, v76
	v_cmp_lt_i32_e64 s[28:29], 3, v76
	v_cmp_lt_i32_e64 s[30:31], 4, v76
	s_waitcnt lgkmcnt(1)
	v_cndmask_b32_e64 v2, 0, v6, s[26:27]
	s_waitcnt lgkmcnt(0)
	v_cndmask_b32_e64 v4, 0, v4, s[28:29]
	s_nop 0
	s_nop 0
	v_lshl_add_u32 v2, v2, 8, v152
	v_lshl_add_u32 v4, v4, 8, v152
	s_nop 0
	ds_bpermute_b32 v6, v90, v30
	s_nop 0
	global_load_dwordx4 v[54:57], v2, s[54:55]
	global_load_dwordx4 v[50:53], v4, s[54:55]
	ds_bpermute_b32 v4, v91, v30
	v_cmp_lt_i32_e64 s[4:5], 5, v76
	s_waitcnt lgkmcnt(1)
	v_cndmask_b32_e64 v2, 0, v6, s[30:31]
	s_nop 0
	v_lshl_add_u32 v2, v2, 8, v152
	s_waitcnt lgkmcnt(0)
	v_cndmask_b32_e64 v4, 0, v4, s[4:5]
	s_nop 0
	ds_bpermute_b32 v6, v92, v30
	s_nop 0
	v_lshl_add_u32 v4, v4, 8, v152
	s_nop 0
	global_load_dwordx4 v[62:65], v2, s[54:55]
	global_load_dwordx4 v[46:49], v4, s[54:55]
	ds_bpermute_b32 v4, v93, v30
	v_cmp_lt_i32_e64 s[2:3], 6, v76
	v_cmp_lt_i32_e32 vcc, 7, v76
	ds_bpermute_b32 v10, v94, v30
	s_waitcnt lgkmcnt(2)
	v_cndmask_b32_e64 v2, 0, v6, s[2:3]
	s_nop 0
	v_lshl_add_u32 v2, v2, 8, v152
	v_mov_b32_e32 v6, v2
	s_waitcnt lgkmcnt(1)
	v_cndmask_b32_e32 v2, 0, v4, vcc
	s_nop 0
	v_lshl_add_u32 v2, v2, 8, v152
	v_mov_b32_e32 v8, v2
	global_load_dwordx4 v[58:61], v6, s[54:55]
	global_load_dwordx4 v[2:5], v8, s[54:55]
	ds_bpermute_b32 v8, v95, v30
	v_cmp_lt_i32_e64 s[6:7], 8, v76
	v_cmp_lt_i32_e64 s[8:9], 9, v76
	ds_bpermute_b32 v14, v96, v30
	ds_bpermute_b32 v16, v97, v30
	s_waitcnt lgkmcnt(3)
	v_cndmask_b32_e64 v6, 0, v10, s[6:7]
	s_waitcnt lgkmcnt(2)
	v_cndmask_b32_e64 v8, 0, v8, s[8:9]
	s_nop 0
	s_nop 0
	v_lshl_add_u32 v6, v6, 8, v152
	v_lshl_add_u32 v8, v8, 8, v152
	s_nop 0
	s_nop 0
	v_cmp_lt_i32_e64 s[10:11], 10, v76
	v_cmp_lt_i32_e64 s[12:13], 11, v76
	ds_bpermute_b32 v22, v98, v30
	ds_bpermute_b32 v24, v99, v30
	global_load_dwordx4 v[10:13], v6, s[54:55]
	s_nop 0
	global_load_dwordx4 v[6:9], v8, s[54:55]
	s_waitcnt lgkmcnt(3)
	v_cndmask_b32_e64 v14, 0, v14, s[10:11]
	s_waitcnt lgkmcnt(2)
	v_cndmask_b32_e64 v16, 0, v16, s[12:13]
	s_nop 0
	s_nop 0
	ds_bpermute_b32 v31, v100, v30
	v_lshl_add_u32 v14, v14, 8, v152
	v_lshl_add_u32 v16, v16, 8, v152
	s_nop 0
	s_nop 0
	v_cmp_lt_i32_e64 s[14:15], 12, v76
	v_cmp_lt_i32_e64 s[16:17], 13, v76
	ds_bpermute_b32 v34, v101, v30
	global_load_dwordx4 v[18:21], v14, s[54:55]
	s_nop 0
	global_load_dwordx4 v[14:17], v16, s[54:55]
	s_waitcnt lgkmcnt(3)
	v_cndmask_b32_e64 v22, 0, v22, s[14:15]
	s_waitcnt lgkmcnt(2)
	v_cndmask_b32_e64 v24, 0, v24, s[16:17]
	s_nop 0
	s_nop 0
	v_cmp_lt_i32_e64 s[22:23], 14, v76
	v_lshl_add_u32 v22, v22, 8, v152
	v_lshl_add_u32 v24, v24, 8, v152
	s_waitcnt lgkmcnt(1)
	v_cndmask_b32_e64 v32, 0, v31, s[22:23]
	s_nop 0
	s_nop 0
	s_nop 0
	v_cmp_lt_i32_e64 s[24:25], 15, v76
	global_load_dwordx4 v[26:29], v22, s[54:55]
	s_nop 0
	global_load_dwordx4 v[22:25], v24, s[54:55]
	v_lshl_add_u32 v30, v32, 8, v152
	s_waitcnt lgkmcnt(0)
	v_cndmask_b32_e64 v32, 0, v34, s[24:25]
	s_nop 0
	v_lshl_add_u32 v32, v32, 8, v152
	s_nop 0
	s_nop 0
	global_load_dwordx4 v[34:37], v30, s[54:55]
	s_nop 0
	global_load_dwordx4 v[30:33], v32, s[54:55]
	s_waitcnt vmcnt(15)
	v_cvt_f32_f16_e32 v72, v42
	v_cvt_f32_f16_sdwa v73, v42 dst_sel:DWORD dst_unused:UNUSED_PAD src0_sel:WORD_1
	v_cvt_f32_f16_e32 v42, v43
	v_cvt_f32_f16_sdwa v43, v43 dst_sel:DWORD dst_unused:UNUSED_PAD src0_sel:WORD_1
	s_waitcnt vmcnt(14)
	v_cvt_f32_f16_e32 v116, v38
	v_cvt_f32_f16_sdwa v117, v38 dst_sel:DWORD dst_unused:UNUSED_PAD src0_sel:WORD_1
	v_cvt_f32_f16_e32 v38, v39
	v_cvt_f32_f16_sdwa v39, v39 dst_sel:DWORD dst_unused:UNUSED_PAD src0_sel:WORD_1
	v_cndmask_b32_e64 v74, 0, 1.0, s[18:19]
	s_waitcnt vmcnt(13)
	v_cvt_f32_f16_e32 v118, v54
	v_cvt_f32_f16_sdwa v119, v54 dst_sel:DWORD dst_unused:UNUSED_PAD src0_sel:WORD_1
	v_cvt_f32_f16_e32 v54, v55
	v_cvt_f32_f16_sdwa v55, v55 dst_sel:DWORD dst_unused:UNUSED_PAD src0_sel:WORD_1
	v_cndmask_b32_e64 v108, 0, 1.0, s[20:21]
	v_pk_fma_f32 v[42:43], v[74:75], v[42:43], 0 op_sel_hi:[0,1,0]
	v_pk_fma_f32 v[38:39], v[108:109], v[38:39], v[42:43] op_sel_hi:[0,1,1]
	s_waitcnt vmcnt(12)
	v_cvt_f32_f16_e32 v42, v51
	v_cvt_f32_f16_sdwa v43, v51 dst_sel:DWORD dst_unused:UNUSED_PAD src0_sel:WORD_1
	v_cndmask_b32_e64 v110, 0, 1.0, s[26:27]
	v_cvt_f32_f16_e32 v120, v50
	v_cvt_f32_f16_sdwa v121, v50 dst_sel:DWORD dst_unused:UNUSED_PAD src0_sel:WORD_1
	s_waitcnt vmcnt(11)
	v_cvt_f32_f16_e32 v50, v63
	v_cvt_f32_f16_sdwa v51, v63 dst_sel:DWORD dst_unused:UNUSED_PAD src0_sel:WORD_1
	v_pk_fma_f32 v[72:73], v[74:75], v[72:73], 0 op_sel_hi:[0,1,0]
	v_pk_fma_f32 v[38:39], v[110:111], v[54:55], v[38:39] op_sel_hi:[0,1,1]
	v_cvt_f32_f16_e32 v54, v44
	v_cvt_f32_f16_sdwa v55, v44 dst_sel:DWORD dst_unused:UNUSED_PAD src0_sel:WORD_1
	v_cndmask_b32_e64 v112, 0, 1.0, s[28:29]
	v_pk_fma_f32 v[72:73], v[108:109], v[116:117], v[72:73] op_sel_hi:[0,1,1]
	v_cvt_f32_f16_e32 v116, v62
	v_cvt_f32_f16_sdwa v117, v62 dst_sel:DWORD dst_unused:UNUSED_PAD src0_sel:WORD_1
	v_cvt_f32_f16_e32 v62, v40
	v_cvt_f32_f16_sdwa v63, v40 dst_sel:DWORD dst_unused:UNUSED_PAD src0_sel:WORD_1
	v_cndmask_b32_e64 v114, 0, 1.0, s[30:31]
	v_pk_fma_f32 v[38:39], v[112:113], v[42:43], v[38:39] op_sel_hi:[0,1,1]
	v_cvt_f32_f16_e32 v42, v56
	v_cvt_f32_f16_sdwa v43, v56 dst_sel:DWORD dst_unused:UNUSED_PAD src0_sel:WORD_1
	v_pk_fma_f32 v[72:73], v[110:111], v[118:119], v[72:73] op_sel_hi:[0,1,1]
	v_pk_fma_f32 v[118:119], v[114:115], v[50:51], v[38:39] op_sel_hi:[0,1,1]
	v_cvt_f32_f16_e32 v50, v52
	v_cvt_f32_f16_sdwa v51, v52 dst_sel:DWORD dst_unused:UNUSED_PAD src0_sel:WORD_1
	v_pk_fma_f32 v[38:39], v[74:75], v[54:55], 0 op_sel_hi:[0,1,0]
	v_cvt_f32_f16_e32 v54, v64
	v_cvt_f32_f16_sdwa v55, v64 dst_sel:DWORD dst_unused:UNUSED_PAD src0_sel:WORD_1
	v_cvt_f32_f16_e32 v44, v45
	v_cvt_f32_f16_sdwa v45, v45 dst_sel:DWORD dst_unused:UNUSED_PAD src0_sel:WORD_1
	v_pk_fma_f32 v[38:39], v[108:109], v[62:63], v[38:39] op_sel_hi:[0,1,1]
	v_pk_fma_f32 v[38:39], v[110:111], v[42:43], v[38:39] op_sel_hi:[0,1,1]
	v_cvt_f32_f16_e32 v40, v41
	v_cvt_f32_f16_sdwa v41, v41 dst_sel:DWORD dst_unused:UNUSED_PAD src0_sel:WORD_1
	v_pk_fma_f32 v[72:73], v[112:113], v[120:121], v[72:73] op_sel_hi:[0,1,1]
	v_pk_fma_f32 v[38:39], v[112:113], v[50:51], v[38:39] op_sel_hi:[0,1,1]
	v_cvt_f32_f16_e32 v42, v57
	v_cvt_f32_f16_sdwa v43, v57 dst_sel:DWORD dst_unused:UNUSED_PAD src0_sel:WORD_1
	v_pk_fma_f32 v[116:117], v[114:115], v[116:117], v[72:73] op_sel_hi:[0,1,1]
	v_pk_fma_f32 v[72:73], v[114:115], v[54:55], v[38:39] op_sel_hi:[0,1,1]
	v_pk_fma_f32 v[38:39], v[74:75], v[44:45], 0 op_sel_hi:[0,1,0]
	v_cvt_f32_f16_e32 v44, v53
	v_cvt_f32_f16_sdwa v45, v53 dst_sel:DWORD dst_unused:UNUSED_PAD src0_sel:WORD_1
	v_cvt_f32_f16_e32 v50, v65
	v_cvt_f32_f16_sdwa v51, v65 dst_sel:DWORD dst_unused:UNUSED_PAD src0_sel:WORD_1
	v_pk_fma_f32 v[38:39], v[108:109], v[40:41], v[38:39] op_sel_hi:[0,1,1]
	v_pk_fma_f32 v[38:39], v[110:111], v[42:43], v[38:39] op_sel_hi:[0,1,1]
	v_pk_fma_f32 v[38:39], v[112:113], v[44:45], v[38:39] op_sel_hi:[0,1,1]
	v_pk_fma_f32 v[50:51], v[114:115], v[50:51], v[38:39] op_sel_hi:[0,1,1]
	s_waitcnt vmcnt(10)
	v_cvt_f32_f16_e32 v38, v46
	v_cvt_f32_f16_sdwa v39, v46 dst_sel:DWORD dst_unused:UNUSED_PAD src0_sel:WORD_1
	s_waitcnt vmcnt(9)
	v_cvt_f32_f16_e32 v112, v58
	v_cvt_f32_f16_sdwa v113, v58 dst_sel:DWORD dst_unused:UNUSED_PAD src0_sel:WORD_1
	v_cvt_f32_f16_e32 v108, v47
	v_cvt_f32_f16_sdwa v109, v47 dst_sel:DWORD dst_unused:UNUSED_PAD src0_sel:WORD_1
	v_cndmask_b32_e64 v52, 0, 1.0, s[4:5]
	v_cvt_f32_f16_e32 v114, v59
	v_cvt_f32_f16_sdwa v115, v59 dst_sel:DWORD dst_unused:UNUSED_PAD src0_sel:WORD_1
	v_cndmask_b32_e64 v64, 0, 1.0, s[2:3]
	s_waitcnt vmcnt(8)
	v_cvt_f32_f16_e32 v122, v2
	v_cvt_f32_f16_sdwa v123, v2 dst_sel:DWORD dst_unused:UNUSED_PAD src0_sel:WORD_1
	v_pk_fma_f32 v[38:39], v[52:53], v[38:39], v[116:117] op_sel_hi:[0,1,1]
	v_cvt_f32_f16_e32 v2, v3
	v_cvt_f32_f16_sdwa v3, v3 dst_sel:DWORD dst_unused:UNUSED_PAD src0_sel:WORD_1
	v_pk_fma_f32 v[38:39], v[64:65], v[112:113], v[38:39] op_sel_hi:[0,1,1]
	s_waitcnt vmcnt(7)
	v_cvt_f32_f16_e32 v112, v10
	v_cvt_f32_f16_sdwa v113, v10 dst_sel:DWORD dst_unused:UNUSED_PAD src0_sel:WORD_1
	v_cvt_f32_f16_e32 v10, v11
	v_cvt_f32_f16_sdwa v11, v11 dst_sel:DWORD dst_unused:UNUSED_PAD src0_sel:WORD_1
	v_pk_fma_f32 v[108:109], v[52:53], v[108:109], v[118:119] op_sel_hi:[0,1,1]
	v_cndmask_b32_e64 v74, 0, 1.0, vcc
	s_waitcnt vmcnt(6)
	v_cvt_f32_f16_e32 v116, v6
	v_cvt_f32_f16_sdwa v117, v6 dst_sel:DWORD dst_unused:UNUSED_PAD src0_sel:WORD_1
	v_pk_fma_f32 v[108:109], v[64:65], v[114:115], v[108:109] op_sel_hi:[0,1,1]
	v_cvt_f32_f16_e32 v6, v7
	v_cvt_f32_f16_sdwa v7, v7 dst_sel:DWORD dst_unused:UNUSED_PAD src0_sel:WORD_1
	v_cvt_f32_f16_e32 v120, v60
	v_cvt_f32_f16_sdwa v121, v60 dst_sel:DWORD dst_unused:UNUSED_PAD src0_sel:WORD_1
	v_cndmask_b32_e64 v60, 0, 1.0, s[6:7]
	v_pk_fma_f32 v[2:3], v[74:75], v[2:3], v[108:109] op_sel_hi:[0,1,1]
	v_pk_fma_f32 v[2:3], v[60:61], v[10:11], v[2:3] op_sel_hi:[0,1,1]
	s_waitcnt vmcnt(5)
	v_cvt_f32_f16_e32 v10, v19
	v_cvt_f32_f16_sdwa v11, v19 dst_sel:DWORD dst_unused:UNUSED_PAD src0_sel:WORD_1
	v_cvt_f32_f16_e32 v110, v48
	v_cvt_f32_f16_sdwa v111, v48 dst_sel:DWORD dst_unused:UNUSED_PAD src0_sel:WORD_1
	v_cndmask_b32_e64 v48, 0, 1.0, s[8:9]
	v_pk_fma_f32 v[2:3], v[48:49], v[6:7], v[2:3] op_sel_hi:[0,1,1]
	s_waitcnt vmcnt(4)
	v_cvt_f32_f16_e32 v6, v15
	v_cvt_f32_f16_sdwa v7, v15 dst_sel:DWORD dst_unused:UNUSED_PAD src0_sel:WORD_1
	v_cndmask_b32_e64 v54, 0, 1.0, s[10:11]
	v_pk_fma_f32 v[2:3], v[54:55], v[10:11], v[2:3] op_sel_hi:[0,1,1]
	s_waitcnt vmcnt(3)
	v_cvt_f32_f16_e32 v10, v27
	v_cvt_f32_f16_sdwa v11, v27 dst_sel:DWORD dst_unused:UNUSED_PAD src0_sel:WORD_1
	v_cndmask_b32_e64 v56, 0, 1.0, s[12:13]
	v_pk_fma_f32 v[2:3], v[56:57], v[6:7], v[2:3] op_sel_hi:[0,1,1]
	s_waitcnt vmcnt(2)
	v_cvt_f32_f16_e32 v6, v23
	v_cvt_f32_f16_sdwa v7, v23 dst_sel:DWORD dst_unused:UNUSED_PAD src0_sel:WORD_1
	v_cndmask_b32_e64 v46, 0, 1.0, s[14:15]
	v_pk_fma_f32 v[2:3], v[46:47], v[10:11], v[2:3] op_sel_hi:[0,1,1]
	s_waitcnt vmcnt(1)
	v_cvt_f32_f16_e32 v10, v35
	v_cvt_f32_f16_sdwa v11, v35 dst_sel:DWORD dst_unused:UNUSED_PAD src0_sel:WORD_1
	v_cndmask_b32_e64 v40, 0, 1.0, s[16:17]
	v_pk_fma_f32 v[2:3], v[40:41], v[6:7], v[2:3] op_sel_hi:[0,1,1]
	s_waitcnt vmcnt(0)
	v_cvt_f32_f16_e32 v6, v31
	v_cvt_f32_f16_sdwa v7, v31 dst_sel:DWORD dst_unused:UNUSED_PAD src0_sel:WORD_1
	v_cndmask_b32_e64 v42, 0, 1.0, s[22:23]
	v_pk_fma_f32 v[2:3], v[42:43], v[10:11], v[2:3] op_sel_hi:[0,1,1]
	v_cvt_f32_f16_e32 v10, v4
	v_cvt_f32_f16_sdwa v11, v4 dst_sel:DWORD dst_unused:UNUSED_PAD src0_sel:WORD_1
	v_cndmask_b32_e64 v44, 0, 1.0, s[24:25]
	v_pk_fma_f32 v[2:3], v[44:45], v[6:7], v[2:3] op_sel_hi:[0,1,1]
	v_pk_fma_f32 v[6:7], v[52:53], v[110:111], v[72:73] op_sel_hi:[0,1,1]
	v_pk_fma_f32 v[6:7], v[64:65], v[120:121], v[6:7] op_sel_hi:[0,1,1]
	v_pk_fma_f32 v[6:7], v[74:75], v[10:11], v[6:7] op_sel_hi:[0,1,1]
	v_cvt_f32_f16_e32 v10, v12
	v_cvt_f32_f16_sdwa v11, v12 dst_sel:DWORD dst_unused:UNUSED_PAD src0_sel:WORD_1
	v_pk_fma_f32 v[38:39], v[74:75], v[122:123], v[38:39] op_sel_hi:[0,1,1]
	v_cvt_f32_f16_e32 v124, v14
	v_cvt_f32_f16_sdwa v125, v14 dst_sel:DWORD dst_unused:UNUSED_PAD src0_sel:WORD_1
	v_cvt_f32_f16_e32 v14, v8
	v_cvt_f32_f16_sdwa v15, v8 dst_sel:DWORD dst_unused:UNUSED_PAD src0_sel:WORD_1
	v_cvt_f32_f16_e32 v122, v18
	v_cvt_f32_f16_sdwa v123, v18 dst_sel:DWORD dst_unused:UNUSED_PAD src0_sel:WORD_1
	v_pk_fma_f32 v[38:39], v[60:61], v[112:113], v[38:39] op_sel_hi:[0,1,1]
	v_cvt_f32_f16_e32 v18, v20
	v_cvt_f32_f16_sdwa v19, v20 dst_sel:DWORD dst_unused:UNUSED_PAD src0_sel:WORD_1
	v_pk_fma_f32 v[38:39], v[48:49], v[116:117], v[38:39] op_sel_hi:[0,1,1]
	v_cvt_f32_f16_e32 v116, v22
	v_cvt_f32_f16_sdwa v117, v22 dst_sel:DWORD dst_unused:UNUSED_PAD src0_sel:WORD_1
	v_cvt_f32_f16_e32 v22, v16
	v_cvt_f32_f16_sdwa v23, v16 dst_sel:DWORD dst_unused:UNUSED_PAD src0_sel:WORD_1
	v_pk_fma_f32 v[6:7], v[60:61], v[10:11], v[6:7] op_sel_hi:[0,1,1]
	v_cvt_f32_f16_e32 v10, v28
	v_cvt_f32_f16_sdwa v11, v28 dst_sel:DWORD dst_unused:UNUSED_PAD src0_sel:WORD_1
	v_cvt_f32_f16_e32 v62, v49
	v_cvt_f32_f16_sdwa v63, v49 dst_sel:DWORD dst_unused:UNUSED_PAD src0_sel:WORD_1
	v_pk_fma_f32 v[6:7], v[48:49], v[14:15], v[6:7] op_sel_hi:[0,1,1]
	v_cvt_f32_f16_e32 v58, v61
	v_cvt_f32_f16_sdwa v59, v61 dst_sel:DWORD dst_unused:UNUSED_PAD src0_sel:WORD_1
	v_pk_fma_f32 v[6:7], v[54:55], v[18:19], v[6:7] op_sel_hi:[0,1,1]
	v_pk_fma_f32 v[6:7], v[56:57], v[22:23], v[6:7] op_sel_hi:[0,1,1]
	v_cvt_f32_f16_e32 v4, v5
	v_cvt_f32_f16_sdwa v5, v5 dst_sel:DWORD dst_unused:UNUSED_PAD src0_sel:WORD_1
	v_pk_fma_f32 v[6:7], v[46:47], v[10:11], v[6:7] op_sel_hi:[0,1,1]
	v_cvt_f32_f16_e32 v10, v13
	v_cvt_f32_f16_sdwa v11, v13 dst_sel:DWORD dst_unused:UNUSED_PAD src0_sel:WORD_1
	v_pk_fma_f32 v[12:13], v[52:53], v[62:63], v[50:51] op_sel_hi:[0,1,1]
	v_cvt_f32_f16_e32 v14, v24
	v_cvt_f32_f16_sdwa v15, v24 dst_sel:DWORD dst_unused:UNUSED_PAD src0_sel:WORD_1
	v_pk_fma_f32 v[12:13], v[64:65], v[58:59], v[12:13] op_sel_hi:[0,1,1]
	v_pk_fma_f32 v[4:5], v[74:75], v[4:5], v[12:13] op_sel_hi:[0,1,1]
	v_cvt_f32_f16_e32 v8, v9
	v_cvt_f32_f16_sdwa v9, v9 dst_sel:DWORD dst_unused:UNUSED_PAD src0_sel:WORD_1
	v_pk_fma_f32 v[4:5], v[60:61], v[10:11], v[4:5] op_sel_hi:[0,1,1]
	v_cvt_f32_f16_e32 v10, v21
	v_cvt_f32_f16_sdwa v11, v21 dst_sel:DWORD dst_unused:UNUSED_PAD src0_sel:WORD_1
	v_cvt_f32_f16_e32 v12, v17
	v_cvt_f32_f16_sdwa v13, v17 dst_sel:DWORD dst_unused:UNUSED_PAD src0_sel:WORD_1
	v_pk_fma_f32 v[6:7], v[40:41], v[14:15], v[6:7] op_sel_hi:[0,1,1]
	v_cvt_f32_f16_e32 v14, v29
	v_cvt_f32_f16_sdwa v15, v29 dst_sel:DWORD dst_unused:UNUSED_PAD src0_sel:WORD_1
	v_pk_fma_f32 v[4:5], v[48:49], v[8:9], v[4:5] op_sel_hi:[0,1,1]
	v_pk_fma_f32 v[4:5], v[54:55], v[10:11], v[4:5] op_sel_hi:[0,1,1]
	v_pk_fma_f32 v[4:5], v[56:57], v[12:13], v[4:5] op_sel_hi:[0,1,1]
	v_cvt_f32_f16_e32 v112, v26
	v_cvt_f32_f16_sdwa v113, v26 dst_sel:DWORD dst_unused:UNUSED_PAD src0_sel:WORD_1
	v_pk_fma_f32 v[4:5], v[46:47], v[14:15], v[4:5] op_sel_hi:[0,1,1]
	ds_bpermute_b32 v15, v81, v76
	ds_bpermute_b32 v16, v85, v76
	v_cvt_f32_f16_e32 v8, v25
	v_cvt_f32_f16_sdwa v9, v25 dst_sel:DWORD dst_unused:UNUSED_PAD src0_sel:WORD_1
	ds_bpermute_b32 v14, v79, v76
	ds_bpermute_b32 v17, v80, v76
	v_pk_fma_f32 v[38:39], v[54:55], v[122:123], v[38:39] op_sel_hi:[0,1,1]
	v_cvt_f32_f16_e32 v122, v34
	v_cvt_f32_f16_sdwa v123, v34 dst_sel:DWORD dst_unused:UNUSED_PAD src0_sel:WORD_1
	v_cvt_f32_f16_e32 v18, v36
	v_cvt_f32_f16_sdwa v19, v36 dst_sel:DWORD dst_unused:UNUSED_PAD src0_sel:WORD_1
	v_cvt_f32_f16_e32 v10, v37
	v_cvt_f32_f16_sdwa v11, v37 dst_sel:DWORD dst_unused:UNUSED_PAD src0_sel:WORD_1
	v_pk_fma_f32 v[38:39], v[56:57], v[124:125], v[38:39] op_sel_hi:[0,1,1]
	v_cvt_f32_f16_e32 v124, v30
	v_cvt_f32_f16_sdwa v125, v30 dst_sel:DWORD dst_unused:UNUSED_PAD src0_sel:WORD_1
	v_cvt_f32_f16_e32 v22, v32
	v_cvt_f32_f16_sdwa v23, v32 dst_sel:DWORD dst_unused:UNUSED_PAD src0_sel:WORD_1
	v_cvt_f32_f16_e32 v12, v33
	v_cvt_f32_f16_sdwa v13, v33 dst_sel:DWORD dst_unused:UNUSED_PAD src0_sel:WORD_1
	v_pk_fma_f32 v[38:39], v[46:47], v[112:113], v[38:39] op_sel_hi:[0,1,1]
	v_pk_fma_f32 v[38:39], v[40:41], v[116:117], v[38:39] op_sel_hi:[0,1,1]
	v_pk_fma_f32 v[4:5], v[40:41], v[8:9], v[4:5] op_sel_hi:[0,1,1]
	s_waitcnt lgkmcnt(2)
	v_max_i32_e32 v8, v15, v16
	v_pk_fma_f32 v[38:39], v[42:43], v[122:123], v[38:39] op_sel_hi:[0,1,1]
	v_pk_fma_f32 v[6:7], v[42:43], v[18:19], v[6:7] op_sel_hi:[0,1,1]
	v_pk_fma_f32 v[4:5], v[42:43], v[10:11], v[4:5] op_sel_hi:[0,1,1]
	s_waitcnt lgkmcnt(0)
	v_max3_i32 v8, v14, v17, v8
	v_pk_fma_f32 v[38:39], v[44:45], v[124:125], v[38:39] op_sel_hi:[0,1,1]
	v_pk_fma_f32 v[6:7], v[44:45], v[22:23], v[6:7] op_sel_hi:[0,1,1]
	v_pk_fma_f32 v[4:5], v[44:45], v[12:13], v[4:5] op_sel_hi:[0,1,1]
	v_cmp_lt_i32_e32 vcc, 16, v8
	s_and_saveexec_b64 s[8:9], vcc
	s_cbranch_execz .LBB2_92
	v_add_u32_e32 v9, v77, v131
	s_mov_b32 s12, 16
	s_mov_b32 s13, 19
	s_mov_b64 s[10:11], 0
